# v3 with 96 converter-role workgroups (160 compute) beside P1/P2 instead of 128
# baseline (speedup 1.0000x reference)
.LBB0_91:
	s_ashr_i32 s2, s70, 3
	s_ashr_i32 s3, s60, 3
	s_add_i32 s2, s2, -12
	s_cmpk_gt_i32 s70, 0xff
	s_cselect_b64 s[0:1], -1, 0
	s_and_b64 s[0:1], s[0:1], s[10:11]
	s_cmp_ge_i32 s3, s2
	s_cselect_b64 s[4:5], -1, 0
	s_and_b64 s[0:1], s[12:13], s[0:1]
	v_writelane_b32 v255, s3, 26
	s_and_b64 s[4:5], s[0:1], s[4:5]
	v_writelane_b32 v255, s4, 27
	s_cmp_gt_i32 s14, 1
	s_nop 0
	v_writelane_b32 v255, s5, 28
	s_cselect_b64 s[4:5], -1, 0
	s_cmp_lt_i32 s15, 2
	s_cselect_b64 s[6:7], -1, 0
	s_or_b64 s[4:5], s[4:5], s[6:7]
	s_and_b64 vcc, exec, s[4:5]
	s_cbranch_vccnz .LBB0_262
	s_cmp_gt_u32 s15, 2
	v_readlane_b32 s4, v255, 27
	s_cselect_b64 s[8:9], -1, 0
	v_readlane_b32 s5, v255, 28
	s_and_b64 s[4:5], s[8:9], s[4:5]
	s_andn2_b64 vcc, exec, s[4:5]
	s_mov_b64 s[4:5], -1
	s_cbranch_vccz .LBB0_148
	v_readlane_b32 s4, v255, 27
	v_readlane_b32 s5, v255, 28
	s_xor_b64 s[4:5], s[4:5], -1
	s_lshl_b32 s2, s2, 3
	s_and_b64 s[0:1], s[0:1], exec
	s_cselect_b32 s2, s2, s70
	s_mov_b64 s[0:1], -1
	s_and_b64 vcc, exec, s[4:5]
	s_cbranch_vccz .LBB0_136
	s_add_u32 s3, s90, 0x28800000
	s_addc_u32 s30, s91, 0
	s_waitcnt vmcnt(11)
	v_mbcnt_lo_u32_b32 v0, -1, 0
	v_mbcnt_hi_u32_b32 v0, -1, v0
	v_readlane_b32 s0, v255, 4
	s_cmpk_lt_i32 s60, 0x300
	s_nop 0
	v_add_u32_e32 v0, s0, v0
	s_cselect_b64 s[0:1], -1, 0
	s_cmpk_gt_i32 s60, 0x2ff
	s_cbranch_scc1 .LBB0_96
	s_ashr_i32 s4, s60, 31
	s_lshr_b32 s4, s4, 29
	s_add_i32 s4, s60, s4
	s_ashr_i32 s5, s4, 3
	s_and_b32 s4, s4, -8
	s_sub_i32 s4, s60, s4
	s_cmp_lt_i32 s4, 0
	s_movk_i32 s6, 0x61
	s_cselect_b32 s6, s6, 0x60
	s_mul_i32 s4, s4, s6
	s_add_i32 s4, s4, s5
	s_mul_hi_i32 s5, s4, 0x2aaaaaab
	s_lshr_b32 s6, s5, 31
	s_ashr_i32 s5, s5, 4
	s_add_i32 s5, s5, s6
	s_mul_i32 s6, s5, 0x60
	s_sub_i32 s6, s4, s6
	s_bfe_i32 s4, s6, 0x80000
	s_bfe_u32 s4, s4, 0x2000d
	s_add_i32 s7, s6, s4
	s_bfe_i32 s4, s7, 0x80000
	s_and_b32 s7, s7, 0xfc
	s_sub_i32 s6, s6, s7
	s_sext_i32_i16 s10, s4
	s_sext_i32_i8 s6, s6
	s_lshr_b32 s4, s10, 2
	s_lshl_b32 s5, s5, 10
	s_lshl_b32 s6, s6, 8
	s_add_i32 s50, s6, s5
	s_bfe_i64 s[4:5], s[4:5], 0x100000
	s_ashr_i32 s49, s10, 2
	s_lshl_b64 s[4:5], s[4:5], 20
	s_add_u32 s22, s3, s4
	s_addc_u32 s23, s30, s5
	s_andn2_b64 vcc, exec, s[0:1]
	s_cbranch_vccz .LBB0_97
	s_branch .LBB0_132
